# baseline (speedup 1.0000x reference)
.LBB2_13:
	v_exp_f32_e32 v48, v48
	v_exp_f32_e32 v49, v49
	v_mfma_f32_32x32x16_bf16 v[112:127], a[192:195], a[128:131], v[16:31]
	ds_read_b64_tr_b16 v[180:181], v223 offset:0
	v_cvt_pk_bf16_f32 v164, v128, v129
	v_exp_f32_e32 v50, v50
	v_exp_f32_e32 v51, v51
	v_mfma_f32_32x32x16_bf16 v[96:111], a[192:195], a[160:163], v[0:15]
	ds_read_b64_tr_b16 v[182:183], v223 offset:0x800
	v_cvt_pk_bf16_f32 v165, v130, v131
	v_mfma_f32_32x32x16_bf16 v[80:95], a[224:227], a[128:131], v[16:31]
	ds_read_b64_tr_b16 v[184:185], v223 offset:0x200
	v_exp_f32_e32 v236, v52
	v_exp_f32_e32 v237, v53
	v_cvt_pk_bf16_f32 v166, v132, v133
	v_mfma_f32_32x32x16_bf16 v[64:79], a[224:227], a[160:163], v[0:15]
	ds_read_b64_tr_b16 v[186:187], v223 offset:0xa00
	ds_read_b64_tr_b16 v[176:177], v223 offset:0x400
	v_exp_f32_e32 v242, v54
	v_exp_f32_e32 v243, v55
	v_cvt_pk_bf16_f32 v167, v134, v135
	v_exp_f32_e32 v198, v56
	v_exp_f32_e32 v199, v57
	v_mfma_f32_32x32x16_bf16 v[112:127], a[196:199], a[132:135], v[112:127]
	ds_read_b64_tr_b16 v[178:179], v223 offset:0xc00
	v_cvt_pk_bf16_f32 v128, v136, v137
	v_exp_f32_e32 v230, v58
	v_exp_f32_e32 v231, v59
	v_mfma_f32_32x32x16_bf16 v[96:111], a[196:199], a[164:167], v[96:111]
	ds_read_b64_tr_b16 v[188:189], v223 offset:0x600
	v_cvt_pk_bf16_f32 v129, v138, v139
	v_exp_f32_e32 v232, v60
	v_exp_f32_e32 v233, v61
	v_mfma_f32_32x32x16_bf16 v[80:95], a[228:231], a[132:135], v[80:95]
	ds_read_b64_tr_b16 v[190:191], v223 offset:0xe00
	v_cvt_pk_bf16_f32 v130, v140, v141
	v_mfma_f32_32x32x16_bf16 v[64:79], a[228:231], a[164:167], v[64:79]
	ds_read_b64_tr_b16 v[172:173], v223 offset:0x1000
	v_exp_f32_e32 v234, v62
	v_exp_f32_e32 v235, v63
	ds_read_b64_tr_b16 v[174:175], v223 offset:0x1800
	v_cvt_pk_bf16_f32 v131, v142, v143
	v_exp_f32_e32 v141, v32
	v_exp_f32_e32 v142, v33
	v_mfma_f32_32x32x16_bf16 v[112:127], a[200:203], a[136:139], v[112:127]
	ds_read_b64_tr_b16 v[168:169], v223 offset:0x1200
	v_cvt_pk_bf16_f32 v192, v144, v145
	v_exp_f32_e32 v143, v34
	v_mfma_f32_32x32x16_bf16 v[96:111], a[200:203], a[168:171], v[96:111]
	ds_read_b64_tr_b16 v[170:171], v223 offset:0x1a00
	v_exp_f32_e32 v244, v35
	v_cvt_pk_bf16_f32 v193, v146, v147
	v_mfma_f32_32x32x16_bf16 v[80:95], a[232:235], a[136:139], v[80:95]
	ds_read_b64_tr_b16 v[160:161], v223 offset:0x1400
	v_exp_f32_e32 v245, v36
	v_exp_f32_e32 v246, v37
	v_cvt_pk_bf16_f32 v194, v148, v149
	v_mfma_f32_32x32x16_bf16 v[64:79], a[232:235], a[168:171], v[64:79]
	ds_read_b64_tr_b16 v[162:163], v223 offset:0x1c00
	ds_read_b64_tr_b16 v[136:137], v223 offset:0x1600
	v_exp_f32_e32 v247, v38
	v_exp_f32_e32 v248, v39
	v_cvt_pk_bf16_f32 v195, v150, v151
	v_exp_f32_e32 v148, v40
	v_exp_f32_e32 v149, v41
	v_mfma_f32_32x32x16_bf16 v[112:127], a[204:207], a[140:143], v[112:127]
	ds_read_b64_tr_b16 v[138:139], v223 offset:0x1e00
	v_cvt_pk_bf16_f32 v144, v152, v153
	v_exp_f32_e32 v150, v42
	v_exp_f32_e32 v151, v43
	v_mfma_f32_32x32x16_bf16 v[96:111], a[204:207], a[172:175], v[96:111]
	ds_read_b64_tr_b16 v[132:133], v223 offset:0x2000
	v_cvt_pk_bf16_f32 v145, v154, v155
	v_exp_f32_e32 v152, v44
	v_exp_f32_e32 v153, v45
	v_mfma_f32_32x32x16_bf16 v[80:95], a[236:239], a[140:143], v[80:95]
	ds_read_b64_tr_b16 v[134:135], v223 offset:0x2800
	v_cvt_pk_bf16_f32 v146, v156, v157
	v_mfma_f32_32x32x16_bf16 v[64:79], a[236:239], a[172:175], v[64:79]
	ds_read_b64_tr_b16 v[60:61], v223 offset:0x2200
	v_exp_f32_e32 v154, v46
	v_exp_f32_e32 v155, v47
	ds_read_b64_tr_b16 v[62:63], v223 offset:0x2a00
	v_cvt_pk_bf16_f32 v147, v158, v159
	s_mov_b32 s0, s30
	v_mfma_f32_32x32x16_bf16 v[112:127], a[208:211], a[144:147], v[112:127]
	ds_read_b64_tr_b16 v[56:57], v223 offset:0x2400
	v_cvt_pk_bf16_f32 v52, v48, v49
	v_add_f32_e32 v32, v239, v48
	v_add_f32_e32 v33, v238, v49
	s_add_i32 s19, s17, 0xfffda000
	s_mov_b32 s1, s19
	v_mfma_f32_32x32x16_bf16 v[96:111], a[208:211], a[176:179], v[96:111]
	ds_read_b64_tr_b16 v[58:59], v223 offset:0x2c00
	v_cvt_pk_bf16_f32 v53, v50, v51
	v_add_f32_e32 v32, v32, v50
	v_add_f32_e32 v33, v33, v51
	s_mov_b32 s81, s37
	v_mfma_f32_32x32x16_bf16 v[80:95], a[240:243], a[144:147], v[80:95]
	ds_read_b64_tr_b16 v[48:49], v223 offset:0x2600
	v_cvt_pk_bf16_f32 v54, v236, v237
	v_add_f32_e32 v32, v32, v236
	v_add_f32_e32 v33, v33, v237
	s_add_i32 s82, s17, 0xfffdc000
	v_mfma_f32_32x32x16_bf16 v[64:79], a[240:243], a[176:179], v[64:79]
	ds_read_b64_tr_b16 v[50:51], v223 offset:0x2e00
	ds_read_b64_tr_b16 v[44:45], v223 offset:0x3000
	v_cvt_pk_bf16_f32 v55, v242, v243
	v_add_f32_e32 v32, v32, v242
	v_add_f32_e32 v33, v33, v243
	s_mov_b32 s83, s39
	v_mfma_f32_32x32x16_bf16 v[112:127], a[212:215], a[148:151], v[112:127]
	ds_read_b64_tr_b16 v[46:47], v223 offset:0x3800
	v_add_f32_e32 v32, v32, v198
	v_add_f32_e32 v33, v33, v199
	s_add_i32 s24, s17, 0xfffde000
	s_mov_b32 s84, s24
	v_mfma_f32_32x32x16_bf16 v[96:111], a[212:215], a[180:183], v[96:111]
	ds_read_b64_tr_b16 v[40:41], v223 offset:0x3200
	v_add_f32_e32 v32, v32, v230
	v_add_f32_e32 v33, v33, v231
	s_mov_b32 s85, s41
	v_mfma_f32_32x32x16_bf16 v[80:95], a[244:247], a[148:151], v[80:95]
	ds_read_b64_tr_b16 v[42:43], v223 offset:0x3a00
	v_add_f32_e32 v32, v32, v232
	v_add_f32_e32 v33, v33, v233
	s_add_i32 s86, s17, 0xfffe0000
	v_mfma_f32_32x32x16_bf16 v[64:79], a[244:247], a[180:183], v[64:79]
	ds_read_b64_tr_b16 v[36:37], v223 offset:0x3400
	ds_read_b64_tr_b16 v[38:39], v223 offset:0x3c00
	v_add_f32_e32 v156, v32, v234
	v_add_f32_e32 v157, v33, v235
	s_mov_b32 s87, s43
	v_mfma_f32_32x32x16_bf16 v[112:127], a[216:219], a[152:155], v[112:127]
	ds_read_b64_tr_b16 v[32:33], v223 offset:0x3600
	v_cvt_pk_bf16_f32 v140, v141, v142
	v_add_f32_e32 v158, v240, v141
	v_add_f32_e32 v142, v241, v142
	s_add_i32 s88, s17, 0xfffba000
	v_mfma_f32_32x32x16_bf16 v[96:111], a[216:219], a[184:187], v[96:111]
	ds_read_b64_tr_b16 v[34:35], v223 offset:0x3e00
	v_cvt_pk_bf16_f32 v141, v143, v244
	v_add_f32_e32 v143, v158, v143
	v_add_f32_e32 v158, v142, v244
	v_mfma_f32_32x32x16_bf16 v[80:95], a[248:251], a[152:155], v[80:95]
	s_mov_b32 s89, s45
	v_cvt_pk_bf16_f32 v142, v245, v246
	v_add_f32_e32 v159, v143, v245
	v_add_f32_e32 v158, v158, v246
	v_mfma_f32_32x32x16_bf16 v[64:79], a[248:251], a[184:187], v[64:79]
	s_add_i32 s90, s17, 0xfffba080
	v_cvt_pk_bf16_f32 v143, v247, v248
	v_add_f32_e32 v159, v159, v247
	v_add_f32_e32 v158, v158, v248
	v_mfma_f32_32x32x16_bf16 v[112:127], a[220:223], a[156:159], v[112:127]
	s_mov_b32 s91, s47
	v_add_f32_e32 v159, v159, v148
	v_add_f32_e32 v158, v158, v149
	v_mfma_f32_32x32x16_bf16 v[96:111], a[220:223], a[188:191], v[96:111]
	s_add_i32 s92, s17, 0xfffbe000
	v_add_f32_e32 v159, v159, v150
	v_add_f32_e32 v158, v158, v151
	v_mfma_f32_32x32x16_bf16 v[80:95], a[252:255], a[156:159], v[80:95]
	s_mov_b32 s93, s49
	v_add_f32_e32 v159, v159, v152
	v_add_f32_e32 v158, v158, v153
	v_mfma_f32_32x32x16_bf16 v[64:79], a[252:255], a[188:191], v[64:79]
	s_add_i32 s94, s17, 0xfffbe080
	v_add_f32_e32 v159, v159, v154
	v_add_f32_e32 v158, v158, v155
	v_add_f32_e32 v156, v156, v157
	v_add_f32_e32 v158, v159, v158
	v_mov_b32_e32 v157, v156
	v_mov_b32_e32 v159, v158
	s_nop 0
	v_permlane32_swap_b32_e32 v156, v157
	v_permlane32_swap_b32_e32 v158, v159
	v_add_f32_e32 v156, v156, v157
	v_add_f32_e32 v158, v158, v159
	v_add_f32_e32 v197, v197, v156
	v_add_f32_e32 v196, v196, v158
	s_waitcnt vmcnt(0) lgkmcnt(0)
	s_barrier
	s_mov_b32 m0, s0
	v_mfma_f32_32x32x16_bf16 a[0:15], v[180:183], v[164:167], a[0:15]
	buffer_load_dwordx4 v209, s[4:7], s1 offen lds
	s_mov_b32 m0, s81
	v_mfma_f32_32x32x16_bf16 a[16:31], v[180:183], v[192:195], a[16:31]
	buffer_load_dwordx4 v210, s[4:7], s82 offen lds
	ds_read_b128 a[192:195], v219 offset:0
	s_mov_b32 m0, s83
	v_mfma_f32_32x32x16_bf16 a[32:47], v[184:187], v[164:167], a[32:47]
	buffer_load_dwordx4 v209, s[4:7], s84 offen lds
	ds_read_b128 a[196:199], v220 offset:0
	s_mov_b32 m0, s85
	v_mfma_f32_32x32x16_bf16 a[48:63], v[184:187], v[192:195], a[48:63]
	buffer_load_dwordx4 v210, s[4:7], s86 offen lds
	ds_read_b128 a[200:203], v221 offset:0
	s_mov_b32 m0, s87
	v_mfma_f32_32x32x16_bf16 a[64:79], v[176:179], v[164:167], a[64:79]
	buffer_load_dwordx4 v211, s[20:23], s88 offen lds
	ds_read_b128 a[204:207], v222 offset:0
	s_mov_b32 m0, s89
	v_mfma_f32_32x32x16_bf16 a[80:95], v[176:179], v[192:195], a[80:95]
	buffer_load_dwordx4 v211, s[20:23], s90 offen lds
	ds_read_b128 a[208:211], v219 offset:128
	s_mov_b32 m0, s91
	v_mfma_f32_32x32x16_bf16 a[96:111], v[188:191], v[164:167], a[96:111]
	buffer_load_dwordx4 v211, s[20:23], s92 offen lds
	ds_read_b128 a[212:215], v220 offset:128
	s_mov_b32 m0, s93
	v_mfma_f32_32x32x16_bf16 a[112:127], v[188:191], v[192:195], a[112:127]
	buffer_load_dwordx4 v211, s[20:23], s94 offen lds
	ds_read_b128 a[216:219], v221 offset:128
	v_mfma_f32_32x32x16_bf16 a[0:15], v[172:175], v[128:131], a[0:15]
	ds_read_b128 a[220:223], v222 offset:128
	v_max3_f32 v156, v112, v113, v80
	v_max3_f32 v157, v114, v115, v81
	v_max3_f32 v156, v156, v82, v83
	v_mfma_f32_32x32x16_bf16 a[16:31], v[172:175], v[144:147], a[16:31]
	ds_read_b128 a[224:227], v219 offset:8192
	v_max3_f32 v156, v156, v116, v117
	v_max3_f32 v157, v157, v118, v119
	v_max3_f32 v156, v156, v84, v85
	v_max3_f32 v157, v157, v86, v87
	v_mfma_f32_32x32x16_bf16 a[32:47], v[168:171], v[128:131], a[32:47]
	ds_read_b128 a[228:231], v220 offset:8192
	v_max3_f32 v156, v156, v120, v121
	v_max3_f32 v157, v157, v122, v123
	v_max3_f32 v156, v156, v88, v89
	v_max3_f32 v157, v157, v90, v91
	v_mfma_f32_32x32x16_bf16 a[48:63], v[168:171], v[144:147], a[48:63]
	ds_read_b128 a[232:235], v221 offset:8192
	v_max3_f32 v156, v156, v124, v125
	v_max3_f32 v157, v157, v126, v127
	v_max3_f32 v156, v156, v92, v93
	v_max3_f32 v157, v157, v94, v95
	v_mfma_f32_32x32x16_bf16 a[64:79], v[160:163], v[128:131], a[64:79]
	ds_read_b128 a[236:239], v222 offset:8192
	v_max3_f32 v158, v96, v97, v64
	v_max3_f32 v159, v98, v99, v65
	v_max3_f32 v158, v158, v66, v67
	v_mfma_f32_32x32x16_bf16 a[80:95], v[160:163], v[144:147], a[80:95]
	ds_read_b128 a[240:243], v219 offset:8320
	v_max3_f32 v158, v158, v100, v101
	v_max3_f32 v159, v159, v102, v103
	v_max3_f32 v158, v158, v68, v69
	v_max3_f32 v159, v159, v70, v71
	v_mfma_f32_32x32x16_bf16 a[96:111], v[136:139], v[128:131], a[96:111]
	ds_read_b128 a[244:247], v220 offset:8320
	v_max3_f32 v128, v158, v104, v105
	v_max3_f32 v129, v159, v106, v107
	v_max3_f32 v128, v128, v72, v73
	v_max3_f32 v129, v129, v74, v75
	v_mfma_f32_32x32x16_bf16 a[112:127], v[136:139], v[144:147], a[112:127]
	ds_read_b128 a[248:251], v221 offset:8320
	v_max3_f32 v128, v128, v108, v109
	v_max3_f32 v129, v129, v110, v111
	v_max3_f32 v128, v128, v76, v77
	v_max3_f32 v130, v129, v78, v79
	v_mfma_f32_32x32x16_bf16 a[0:15], v[132:135], v[52:55], a[0:15]
	ds_read_b128 a[252:255], v222 offset:8320
	v_max_f32_e32 v129, v156, v157
	v_max_f32_e32 v128, v128, v130
	v_mov_b32_e32 v131, v129
	v_mov_b32_e32 v130, v128
	v_mfma_f32_32x32x16_bf16 a[16:31], v[132:135], v[140:143], a[16:31]
	v_permlane32_swap_b32_e32 v129, v131
	v_permlane32_swap_b32_e32 v128, v130
	v_max_f32_e32 v129, v129, v131
	v_max_f32_e32 v128, v128, v130
	v_max_f32_e32 v130, v129, v128
	v_mfma_f32_32x32x16_bf16 a[32:47], v[60:63], v[52:55], a[32:47]
	v_cmp_lt_f32_e32 vcc, s79, v130
	s_cmp_lg_u64 vcc, 0
	s_cselect_b64 s[0:1], -1, 0
	s_cbranch_vccnz .LBB2_18

.LBB2_15:
	s_waitcnt lgkmcnt(0)
	v_exp_f32_e32 v80, v80
	v_exp_f32_e32 v81, v81
	v_mfma_f32_32x32x16_bf16 v[112:127], a[192:195], a[128:131], v[16:31]
	ds_read_b64_tr_b16 v[180:181], v208 offset:0
	v_cvt_pk_bf16_f32 v164, v128, v129
	v_exp_f32_e32 v82, v82
	v_exp_f32_e32 v83, v83
	v_mfma_f32_32x32x16_bf16 v[96:111], a[192:195], a[160:163], v[0:15]
	ds_read_b64_tr_b16 v[182:183], v208 offset:0x800
	v_cvt_pk_bf16_f32 v165, v130, v131
	v_mfma_f32_32x32x16_bf16 v[48:63], a[224:227], a[128:131], v[16:31]
	ds_read_b64_tr_b16 v[184:185], v208 offset:0x200
	v_exp_f32_e32 v240, v84
	v_exp_f32_e32 v241, v85
	v_cvt_pk_bf16_f32 v166, v132, v133
	v_mfma_f32_32x32x16_bf16 v[32:47], a[224:227], a[160:163], v[0:15]
	ds_read_b64_tr_b16 v[186:187], v208 offset:0xa00
	ds_read_b64_tr_b16 v[176:177], v208 offset:0x400
	v_exp_f32_e32 v242, v86
	v_exp_f32_e32 v243, v87
	v_cvt_pk_bf16_f32 v167, v134, v135
	v_exp_f32_e32 v198, v88
	v_exp_f32_e32 v199, v89
	v_mfma_f32_32x32x16_bf16 v[112:127], a[196:199], a[132:135], v[112:127]
	ds_read_b64_tr_b16 v[178:179], v208 offset:0xc00
	v_cvt_pk_bf16_f32 v128, v136, v137
	v_exp_f32_e32 v230, v90
	v_exp_f32_e32 v231, v91
	v_mfma_f32_32x32x16_bf16 v[96:111], a[196:199], a[164:167], v[96:111]
	ds_read_b64_tr_b16 v[188:189], v208 offset:0x600
	v_cvt_pk_bf16_f32 v129, v138, v139
	v_exp_f32_e32 v232, v92
	v_exp_f32_e32 v233, v93
	v_mfma_f32_32x32x16_bf16 v[48:63], a[228:231], a[132:135], v[48:63]
	ds_read_b64_tr_b16 v[190:191], v208 offset:0xe00
	v_cvt_pk_bf16_f32 v130, v140, v141
	v_mfma_f32_32x32x16_bf16 v[32:47], a[228:231], a[164:167], v[32:47]
	ds_read_b64_tr_b16 v[172:173], v208 offset:0x1000
	v_exp_f32_e32 v234, v94
	v_exp_f32_e32 v235, v95
	ds_read_b64_tr_b16 v[174:175], v208 offset:0x1800
	v_cvt_pk_bf16_f32 v131, v142, v143
	v_exp_f32_e32 v141, v64
	v_exp_f32_e32 v142, v65
	v_mfma_f32_32x32x16_bf16 v[112:127], a[200:203], a[136:139], v[112:127]
	ds_read_b64_tr_b16 v[168:169], v208 offset:0x1200
	v_cvt_pk_bf16_f32 v192, v144, v145
	v_exp_f32_e32 v143, v66
	v_mfma_f32_32x32x16_bf16 v[96:111], a[200:203], a[168:171], v[96:111]
	ds_read_b64_tr_b16 v[170:171], v208 offset:0x1a00
	v_exp_f32_e32 v244, v67
	v_cvt_pk_bf16_f32 v193, v146, v147
	v_mfma_f32_32x32x16_bf16 v[48:63], a[232:235], a[136:139], v[48:63]
	ds_read_b64_tr_b16 v[160:161], v208 offset:0x1400
	v_exp_f32_e32 v245, v68
	v_exp_f32_e32 v246, v69
	v_cvt_pk_bf16_f32 v194, v148, v149
	v_mfma_f32_32x32x16_bf16 v[32:47], a[232:235], a[168:171], v[32:47]
	ds_read_b64_tr_b16 v[162:163], v208 offset:0x1c00
	ds_read_b64_tr_b16 v[136:137], v208 offset:0x1600
	v_exp_f32_e32 v247, v70
	v_exp_f32_e32 v248, v71
	v_cvt_pk_bf16_f32 v195, v150, v151
	v_exp_f32_e32 v148, v72
	v_exp_f32_e32 v149, v73
	v_mfma_f32_32x32x16_bf16 v[112:127], a[204:207], a[140:143], v[112:127]
	ds_read_b64_tr_b16 v[138:139], v208 offset:0x1e00
	v_cvt_pk_bf16_f32 v144, v152, v153
	v_exp_f32_e32 v150, v74
	v_exp_f32_e32 v151, v75
	v_mfma_f32_32x32x16_bf16 v[96:111], a[204:207], a[172:175], v[96:111]
	ds_read_b64_tr_b16 v[132:133], v208 offset:0x2000
	v_cvt_pk_bf16_f32 v145, v154, v155
	v_exp_f32_e32 v152, v76
	v_exp_f32_e32 v153, v77
	v_mfma_f32_32x32x16_bf16 v[48:63], a[236:239], a[140:143], v[48:63]
	ds_read_b64_tr_b16 v[134:135], v208 offset:0x2800
	v_cvt_pk_bf16_f32 v146, v156, v157
	v_mfma_f32_32x32x16_bf16 v[32:47], a[236:239], a[172:175], v[32:47]
	ds_read_b64_tr_b16 v[92:93], v208 offset:0x2200
	v_exp_f32_e32 v154, v78
	v_exp_f32_e32 v155, v79
	ds_read_b64_tr_b16 v[94:95], v208 offset:0x2a00
	v_cvt_pk_bf16_f32 v147, v158, v159
	s_mov_b32 s0, s51
	v_mfma_f32_32x32x16_bf16 v[112:127], a[208:211], a[144:147], v[112:127]
	ds_read_b64_tr_b16 v[88:89], v208 offset:0x2400
	v_cvt_pk_bf16_f32 v84, v80, v81
	v_add_f32_e32 v64, v237, v80
	v_add_f32_e32 v65, v236, v81
	s_add_i32 s1, s17, 0xffffa000
	v_mfma_f32_32x32x16_bf16 v[96:111], a[208:211], a[176:179], v[96:111]
	ds_read_b64_tr_b16 v[90:91], v208 offset:0x2c00
	v_cvt_pk_bf16_f32 v85, v82, v83
	v_add_f32_e32 v64, v64, v82
	v_add_f32_e32 v65, v65, v83
	s_mov_b32 s81, s53
	v_mfma_f32_32x32x16_bf16 v[48:63], a[240:243], a[144:147], v[48:63]
	ds_read_b64_tr_b16 v[80:81], v208 offset:0x2600
	v_cvt_pk_bf16_f32 v86, v240, v241
	v_add_f32_e32 v64, v64, v240
	v_add_f32_e32 v65, v65, v241
	s_add_i32 s82, s17, 0xffffc000
	v_mfma_f32_32x32x16_bf16 v[32:47], a[240:243], a[176:179], v[32:47]
	ds_read_b64_tr_b16 v[82:83], v208 offset:0x2e00
	ds_read_b64_tr_b16 v[76:77], v208 offset:0x3000
	v_cvt_pk_bf16_f32 v87, v242, v243
	v_add_f32_e32 v64, v64, v242
	v_add_f32_e32 v65, v65, v243
	s_mov_b32 s83, s55
	v_mfma_f32_32x32x16_bf16 v[112:127], a[212:215], a[148:151], v[112:127]
	ds_read_b64_tr_b16 v[78:79], v208 offset:0x3800
	v_add_f32_e32 v64, v64, v198
	v_add_f32_e32 v65, v65, v199
	s_add_i32 s84, s17, 0xffffe000
	v_mfma_f32_32x32x16_bf16 v[96:111], a[212:215], a[180:183], v[96:111]
	ds_read_b64_tr_b16 v[72:73], v208 offset:0x3200
	v_add_f32_e32 v64, v64, v230
	v_add_f32_e32 v65, v65, v231
	s_mov_b32 s85, s57
	v_mfma_f32_32x32x16_bf16 v[48:63], a[244:247], a[148:151], v[48:63]
	ds_read_b64_tr_b16 v[74:75], v208 offset:0x3a00
	v_add_f32_e32 v64, v64, v232
	v_add_f32_e32 v65, v65, v233
	s_mov_b32 s86, s17
	v_mfma_f32_32x32x16_bf16 v[32:47], a[244:247], a[180:183], v[32:47]
	ds_read_b64_tr_b16 v[68:69], v208 offset:0x3400
	ds_read_b64_tr_b16 v[70:71], v208 offset:0x3c00
	v_add_f32_e32 v156, v64, v234
	v_add_f32_e32 v157, v65, v235
	s_mov_b32 s87, s31
	v_mfma_f32_32x32x16_bf16 v[112:127], a[216:219], a[152:155], v[112:127]
	ds_read_b64_tr_b16 v[64:65], v208 offset:0x3600
	v_cvt_pk_bf16_f32 v140, v141, v142
	v_add_f32_e32 v158, v238, v141
	v_add_f32_e32 v142, v239, v142
	v_mfma_f32_32x32x16_bf16 v[96:111], a[216:219], a[184:187], v[96:111]
	ds_read_b64_tr_b16 v[66:67], v208 offset:0x3e00
	v_cvt_pk_bf16_f32 v141, v143, v244
	v_add_f32_e32 v143, v158, v143
	v_add_f32_e32 v158, v142, v244
	v_mfma_f32_32x32x16_bf16 v[48:63], a[248:251], a[152:155], v[48:63]
	s_mov_b32 s88, s59
	v_cvt_pk_bf16_f32 v142, v245, v246
	v_add_f32_e32 v159, v143, v245
	v_add_f32_e32 v158, v158, v246
	v_mfma_f32_32x32x16_bf16 v[32:47], a[248:251], a[184:187], v[32:47]
	s_add_i32 s89, s17, 0xfffda080
	v_cvt_pk_bf16_f32 v143, v247, v248
	v_add_f32_e32 v159, v159, v247
	v_add_f32_e32 v158, v158, v248
	v_mfma_f32_32x32x16_bf16 v[112:127], a[220:223], a[156:159], v[112:127]
	s_mov_b32 s90, s61
	v_add_f32_e32 v159, v159, v148
	v_add_f32_e32 v158, v158, v149
	v_mfma_f32_32x32x16_bf16 v[96:111], a[220:223], a[188:191], v[96:111]
	v_add_f32_e32 v159, v159, v150
	v_add_f32_e32 v158, v158, v151
	v_mfma_f32_32x32x16_bf16 v[48:63], a[252:255], a[156:159], v[48:63]
	s_mov_b32 s91, s62
	v_add_f32_e32 v159, v159, v152
	v_add_f32_e32 v158, v158, v153
	v_mfma_f32_32x32x16_bf16 v[32:47], a[252:255], a[188:191], v[32:47]
	s_add_i32 s92, s17, 0xfffde080
	v_add_f32_e32 v159, v159, v154
	v_add_f32_e32 v158, v158, v155
	v_add_f32_e32 v156, v156, v157
	v_add_f32_e32 v158, v159, v158
	v_mov_b32_e32 v157, v156
	v_mov_b32_e32 v159, v158
	s_nop 0
	v_permlane32_swap_b32_e32 v156, v157
	v_permlane32_swap_b32_e32 v158, v159
	v_add_f32_e32 v156, v156, v157
	v_add_f32_e32 v158, v158, v159
	v_add_f32_e32 v197, v197, v156
	v_add_f32_e32 v196, v196, v158
	s_waitcnt vmcnt(0) lgkmcnt(0)
	s_barrier
	s_mov_b32 m0, s0
	v_mfma_f32_32x32x16_bf16 a[0:15], v[180:183], v[164:167], a[0:15]
	buffer_load_dwordx4 v209, s[4:7], s1 offen lds
	s_mov_b32 m0, s81
	v_mfma_f32_32x32x16_bf16 a[16:31], v[180:183], v[192:195], a[16:31]
	buffer_load_dwordx4 v210, s[4:7], s82 offen lds
	ds_read_b128 a[192:195], v204 offset:0
	s_mov_b32 m0, s83
	v_mfma_f32_32x32x16_bf16 a[32:47], v[184:187], v[164:167], a[32:47]
	buffer_load_dwordx4 v209, s[4:7], s84 offen lds
	ds_read_b128 a[196:199], v205 offset:0
	s_mov_b32 m0, s85
	v_mfma_f32_32x32x16_bf16 a[48:63], v[184:187], v[192:195], a[48:63]
	buffer_load_dwordx4 v210, s[4:7], s86 offen lds
	ds_read_b128 a[200:203], v206 offset:0
	s_mov_b32 m0, s87
	v_mfma_f32_32x32x16_bf16 a[64:79], v[176:179], v[164:167], a[64:79]
	buffer_load_dwordx4 v211, s[20:23], s19 offen lds
	ds_read_b128 a[204:207], v207 offset:0
	s_mov_b32 m0, s88
	v_mfma_f32_32x32x16_bf16 a[80:95], v[176:179], v[192:195], a[80:95]
	buffer_load_dwordx4 v211, s[20:23], s89 offen lds
	ds_read_b128 a[208:211], v204 offset:128
	s_mov_b32 m0, s90
	v_mfma_f32_32x32x16_bf16 a[96:111], v[188:191], v[164:167], a[96:111]
	buffer_load_dwordx4 v211, s[20:23], s24 offen lds
	ds_read_b128 a[212:215], v205 offset:128
	s_mov_b32 m0, s91
	v_mfma_f32_32x32x16_bf16 a[112:127], v[188:191], v[192:195], a[112:127]
	buffer_load_dwordx4 v211, s[20:23], s92 offen lds
	ds_read_b128 a[216:219], v206 offset:128
	v_mfma_f32_32x32x16_bf16 a[0:15], v[172:175], v[128:131], a[0:15]
	ds_read_b128 a[220:223], v207 offset:128
	v_max3_f32 v156, v112, v113, v48
	v_max3_f32 v157, v114, v115, v49
	v_max3_f32 v156, v156, v50, v51
	v_mfma_f32_32x32x16_bf16 a[16:31], v[172:175], v[144:147], a[16:31]
	ds_read_b128 a[224:227], v204 offset:8192
	v_max3_f32 v156, v156, v116, v117
	v_max3_f32 v157, v157, v118, v119
	v_max3_f32 v156, v156, v52, v53
	v_max3_f32 v157, v157, v54, v55
	v_mfma_f32_32x32x16_bf16 a[32:47], v[168:171], v[128:131], a[32:47]
	ds_read_b128 a[228:231], v205 offset:8192
	v_max3_f32 v156, v156, v120, v121
	v_max3_f32 v157, v157, v122, v123
	v_max3_f32 v156, v156, v56, v57
	v_max3_f32 v157, v157, v58, v59
	v_mfma_f32_32x32x16_bf16 a[48:63], v[168:171], v[144:147], a[48:63]
	ds_read_b128 a[232:235], v206 offset:8192
	v_max3_f32 v156, v156, v124, v125
	v_max3_f32 v157, v157, v126, v127
	v_max3_f32 v156, v156, v60, v61
	v_max3_f32 v157, v157, v62, v63
	v_mfma_f32_32x32x16_bf16 a[64:79], v[160:163], v[128:131], a[64:79]
	ds_read_b128 a[236:239], v207 offset:8192
	v_max3_f32 v158, v96, v97, v32
	v_max3_f32 v159, v98, v99, v33
	v_max3_f32 v158, v158, v34, v35
	v_mfma_f32_32x32x16_bf16 a[80:95], v[160:163], v[144:147], a[80:95]
	ds_read_b128 a[240:243], v204 offset:8320
	v_max3_f32 v158, v158, v100, v101
	v_max3_f32 v159, v159, v102, v103
	v_max3_f32 v158, v158, v36, v37
	v_max3_f32 v159, v159, v38, v39
	v_mfma_f32_32x32x16_bf16 a[96:111], v[136:139], v[128:131], a[96:111]
	ds_read_b128 a[244:247], v205 offset:8320
	v_max3_f32 v128, v158, v104, v105
	v_max3_f32 v129, v159, v106, v107
	v_max3_f32 v128, v128, v40, v41
	v_max3_f32 v129, v129, v42, v43
	v_mfma_f32_32x32x16_bf16 a[112:127], v[136:139], v[144:147], a[112:127]
	ds_read_b128 a[248:251], v206 offset:8320
	v_max3_f32 v128, v128, v108, v109
	v_max3_f32 v129, v129, v110, v111
	v_max3_f32 v128, v128, v44, v45
	v_max3_f32 v130, v129, v46, v47
	v_mfma_f32_32x32x16_bf16 a[0:15], v[132:135], v[84:87], a[0:15]
	ds_read_b128 a[252:255], v207 offset:8320
	v_max_f32_e32 v129, v156, v157
	v_max_f32_e32 v128, v128, v130
	v_mov_b32_e32 v131, v129
	v_mov_b32_e32 v130, v128
	v_mfma_f32_32x32x16_bf16 a[16:31], v[132:135], v[140:143], a[16:31]
	v_permlane32_swap_b32_e32 v129, v131
	v_permlane32_swap_b32_e32 v128, v130
	v_max_f32_e32 v129, v129, v131
	v_max_f32_e32 v128, v128, v130
	v_max_f32_e32 v130, v129, v128
	v_mfma_f32_32x32x16_bf16 a[32:47], v[92:95], v[84:87], a[32:47]
	v_cmp_lt_f32_e32 vcc, s79, v130
	s_cmp_lg_u64 vcc, 0
	s_cselect_b64 s[0:1], -1, 0
	s_cbranch_vccnz .LBB2_20
